# mLSTM conversion: the 32 tiles of a wave spread over all 36 chunks (none in chunks 8,17,26,35), second slot dropped
# speedup vs baseline: 1.0030x; 1.0030x over previous
; __device__ __forceinline__ void mlstm_unit(LAS unsigned char* lds, const bf16_t* __restrict__ PM, const float* __restrict__ GATES, bf16_t* __restrict__ Hout,
;                                            int b, int h, int dir, int vs, Conv& cvs, const int wave_) {
;     ...
;         if (ci + 1 < 36) ML_LOAD(ci + 1);
;         CV_ISSUE();
.LBB0_567:
	s_mul_i32 s100, s57, 0x38e38e39
	s_cmp_le_u32 s100, 0x1c71c71c
	s_cselect_b32 s100, 0, s101
	s_cmp_lt_i32 s33, s100
	s_cselect_b64 s[92:93], -1, 0
	s_cmp_ge_i32 s33, s100
	s_cbranch_scc1 .LBB0_574
	s_cmp_gt_i32 s33, 0xffff
	s_mov_b64 s[2:3], -1
	s_cbranch_scc0 .LBB0_570
	s_add_i32 s2, s33, 0xffff0000
	s_lshr_b32 s2, s2, 10
	s_mov_b32 s3, s79
	v_readlane_b32 s40, v254, 34
	s_lshl_b64 s[2:3], s[2:3], 24
	v_readlane_b32 s48, v254, 42
	v_readlane_b32 s49, v254, 43
	s_add_u32 s72, s48, s2
	v_readlane_b32 s41, v254, 35
	v_readlane_b32 s42, v254, 36
	v_readlane_b32 s43, v254, 37
	v_readlane_b32 s44, v254, 38
	v_readlane_b32 s45, v254, 39
	v_readlane_b32 s46, v254, 40
	v_readlane_b32 s47, v254, 41
	v_readlane_b32 s50, v254, 44
	v_readlane_b32 s51, v254, 45
	v_readlane_b32 s52, v254, 46
	v_readlane_b32 s53, v254, 47
	v_readlane_b32 s54, v254, 48
	v_readlane_b32 s55, v254, 49
	s_addc_u32 s73, s49, s3
	s_lshl_b32 s37, s33, 1
	s_mov_b64 s[2:3], 0

; __device__ __forceinline__ void mlstm_unit(LAS unsigned char* lds, const bf16_t* __restrict__ PM, const float* __restrict__ GATES, bf16_t* __restrict__ Hout,
;                                            int b, int h, int dir, int vs, Conv& cvs, const int wave_) {
;     ...
;         CV_FINISH();
;         if ((ci % 3) == 0) { CV_ISSUE(); pend_b = true; }
.Lcv_noinc:
	s_mov_b64 s[30:31], 0
	s_cmp_lt_i32 s33, s101
	s_cselect_b64 s[2:3], -1, 0
	s_and_b64 s[2:3], s[30:31], s[2:3]
	s_andn2_b64 vcc, exec, s[2:3]
	s_cbranch_vccnz .LBB0_615
	s_cmp_gt_i32 s33, 0xffff
	s_mov_b64 s[2:3], -1
	s_cbranch_scc0 .LBB0_611
	s_add_i32 s0, s33, 0xffff0000
	s_lshr_b32 s2, s0, 10
	s_mov_b32 s3, s79
	v_readlane_b32 s36, v254, 34
	s_lshl_b64 s[2:3], s[2:3], 24
	v_readlane_b32 s44, v254, 42
	v_readlane_b32 s45, v254, 43
	s_add_u32 s72, s44, s2
	v_readlane_b32 s37, v254, 35
	v_readlane_b32 s38, v254, 36
	v_readlane_b32 s39, v254, 37
	v_readlane_b32 s40, v254, 38
	v_readlane_b32 s41, v254, 39
	v_readlane_b32 s42, v254, 40
	v_readlane_b32 s43, v254, 41
	v_readlane_b32 s46, v254, 44
	v_readlane_b32 s47, v254, 45
	v_readlane_b32 s48, v254, 46
	v_readlane_b32 s49, v254, 47
	v_readlane_b32 s50, v254, 48
	v_readlane_b32 s51, v254, 49
	s_addc_u32 s73, s45, s3
	s_lshl_b32 s0, s33, 1
	s_mov_b64 s[2:3], 0
